# P0 sections: silu(cond) staging with 8 loads in flight, adaLN GEMV first 8 row loads of each batch issued together (counted waits)
# baseline (speedup 1.0000x reference)
.LBB0_18:
	s_mov_b64 s[8:9], 0x1000
	v_lshl_add_u64 v[14:15], v[0:1], 0, s[8:9]
	s_mov_b64 s[8:9], 0x2000
	v_lshl_add_u64 v[16:17], v[0:1], 0, s[8:9]
	s_mov_b64 s[8:9], 0x3000
	v_lshl_add_u64 v[18:19], v[0:1], 0, s[8:9]
	global_load_dword v4, v[0:1], off
	global_load_dword v5, v[0:1], off offset:2048
	global_load_dword v6, v[14:15], off
	global_load_dword v7, v[14:15], off offset:2048
	global_load_dword v8, v[16:17], off
	global_load_dword v9, v[16:17], off offset:2048
	global_load_dword v12, v[18:19], off
	global_load_dword v13, v[18:19], off offset:2048
	s_waitcnt vmcnt(0)
	v_mul_f32_e32 v20, 0xbfb8aa3b, v4
	v_exp_f32_e32 v20, v20
	s_nop 0
	v_add_f32_e32 v20, 1.0, v20
	v_rcp_f32_e32 v20, v20
	s_nop 0
	v_mul_f32_e32 v4, v4, v20
	ds_write_b32 v3, v4
	v_mul_f32_e32 v20, 0xbfb8aa3b, v5
	v_exp_f32_e32 v20, v20
	s_nop 0
	v_add_f32_e32 v20, 1.0, v20
	v_rcp_f32_e32 v20, v20
	s_nop 0
	v_mul_f32_e32 v5, v5, v20
	ds_write_b32 v3, v5 offset:2048
	v_mul_f32_e32 v20, 0xbfb8aa3b, v6
	v_exp_f32_e32 v20, v20
	s_nop 0
	v_add_f32_e32 v20, 1.0, v20
	v_rcp_f32_e32 v20, v20
	s_nop 0
	v_mul_f32_e32 v6, v6, v20
	ds_write_b32 v3, v6 offset:4096
	v_mul_f32_e32 v20, 0xbfb8aa3b, v7
	v_exp_f32_e32 v20, v20
	s_nop 0
	v_add_f32_e32 v20, 1.0, v20
	v_rcp_f32_e32 v20, v20
	s_nop 0
	v_mul_f32_e32 v7, v7, v20
	ds_write_b32 v3, v7 offset:6144
	v_mul_f32_e32 v20, 0xbfb8aa3b, v8
	v_exp_f32_e32 v20, v20
	s_nop 0
	v_add_f32_e32 v20, 1.0, v20
	v_rcp_f32_e32 v20, v20
	s_nop 0
	v_mul_f32_e32 v8, v8, v20
	ds_write_b32 v3, v8 offset:8192
	v_mul_f32_e32 v20, 0xbfb8aa3b, v9
	v_exp_f32_e32 v20, v20
	s_nop 0
	v_add_f32_e32 v20, 1.0, v20
	v_rcp_f32_e32 v20, v20
	s_nop 0
	v_mul_f32_e32 v9, v9, v20
	ds_write_b32 v3, v9 offset:10240
	v_mul_f32_e32 v20, 0xbfb8aa3b, v12
	v_exp_f32_e32 v20, v20
	s_nop 0
	v_add_f32_e32 v20, 1.0, v20
	v_rcp_f32_e32 v20, v20
	s_nop 0
	v_mul_f32_e32 v12, v12, v20
	ds_write_b32 v3, v12 offset:12288
	v_mul_f32_e32 v20, 0xbfb8aa3b, v13
	v_exp_f32_e32 v20, v20
	s_nop 0
	v_add_f32_e32 v20, 1.0, v20
	v_rcp_f32_e32 v20, v20
	s_nop 0
	v_mul_f32_e32 v13, v13, v20
	ds_write_b32 v3, v13 offset:14336

.LBB0_24:
	v_lshl_add_u64 v[104:105], v[102:103], 0, s[96:97]
	s_mov_b32 s4, 0xc000
	global_load_dwordx2 v[200:201], v[104:105], off
	v_add_co_u32_e64 v154, s[48:49], s88, v104
	v_add_co_u32_e64 v156, s[50:51], s4, v104
	v_mov_b32_e32 v107, s1
	v_addc_co_u32_e64 v155, s[48:49], 0, v105, s[48:49]
	v_addc_co_u32_e64 v157, s[50:51], 0, v105, s[50:51]
	ds_read_b128 v[44:47], v107
	ds_read_b128 v[72:75], v107 offset:16
	ds_read_b128 v[40:43], v107 offset:32
	ds_read_b128 v[4:7], v107 offset:48
	ds_read_b128 v[48:51], v107 offset:4096
	ds_read_b128 v[86:89], v107 offset:4112
	ds_read_b128 v[52:55], v107 offset:8192
	ds_read_b128 v[76:79], v107 offset:8208
	ds_read_b128 v[60:63], v107 offset:12288
	ds_read_b128 v[82:85], v107 offset:12304
	ds_read_b128 v[68:71], v107 offset:4128
	ds_read_b128 v[64:67], v107 offset:8224
	ds_read_b128 v[56:59], v107 offset:12320
	ds_read_b128 v[32:35], v107 offset:4144
	ds_read_b128 v[24:27], v107 offset:8240
	ds_read_b128 v[0:3], v107 offset:12336
	ds_read_b128 v[8:11], v107 offset:64
	ds_read_b128 v[12:15], v107 offset:4160
	ds_read_b128 v[16:19], v107 offset:8256
	ds_read_b128 v[20:23], v107 offset:12352
	global_load_dwordx2 v[202:203], v[154:155], off
	s_nop 0
	global_load_dwordx2 v[204:205], v[156:157], off
	s_mov_b32 s4, 0x12000
	v_add_co_u32_e64 v158, s[52:53], s4, v104
	s_mov_b32 s4, 0x18000
	s_nop 0
	v_addc_co_u32_e64 v159, s[52:53], 0, v105, s[52:53]
	v_add_co_u32_e64 v80, s[54:55], s4, v104
	s_mov_b32 s4, 0x1e000
	v_add_co_u32_e64 v92, s[56:57], s4, v104
	s_mov_b32 s4, 0x24000
	v_add_co_u32_e64 v94, s[58:59], s4, v104
	v_addc_co_u32_e64 v81, s[54:55], 0, v105, s[54:55]
	s_waitcnt lgkmcnt(14)
	v_mov_b32_e32 v162, v47
	v_mov_b32_e32 v168, v51
	v_addc_co_u32_e64 v93, s[56:57], 0, v105, s[56:57]
	v_addc_co_u32_e64 v95, s[56:57], 0, v105, s[58:59]
	s_mov_b32 s4, 0x2a000
	v_add_co_u32_e64 v90, s[46:47], s4, v104
	s_mov_b32 s4, 0x30000
	s_nop 0
	v_addc_co_u32_e64 v91, s[46:47], 0, v105, s[46:47]
	s_nop 0
	global_load_dwordx2 v[206:207], v[158:159], off
	global_load_dwordx2 v[208:209], v[80:81], off
	global_load_dwordx2 v[210:211], v[92:93], off
	global_load_dwordx2 v[212:213], v[94:95], off
	global_load_dwordx2 v[214:215], v[90:91], off
	s_mov_b32 s6, 0x36000
	s_mov_b32 s8, 0x3c000
	s_mov_b32 s10, 0x42000
	s_mov_b32 s12, 0x48000
	s_mov_b32 s14, 0x4e000
	s_mov_b32 s16, 0x54000
	s_mov_b32 s18, 0x5a000
	s_mov_b32 s20, 0x60000
	s_mov_b32 s22, 0x66000
	s_mov_b32 s24, 0x6c000
	s_mov_b32 s26, 0x72000
	s_mov_b32 s28, 0x78000
	s_mov_b32 s30, 0x7e000
	s_mov_b32 s34, 0x84000
	s_mov_b32 s36, 0x8a000
	s_mov_b32 s38, 0x90000
	s_mov_b32 s40, 0x96000
	s_mov_b32 s42, 0x9c000
	s_mov_b32 s44, 0xa2000
	s_mov_b32 s48, 0xa8000
	s_mov_b32 s50, 0xae000
	s_mov_b32 s52, 0xb4000
	s_mov_b32 s54, 0xba000
	v_add_co_u32_e64 v106, s[4:5], s4, v104
	v_add_co_u32_e64 v108, s[6:7], s6, v104
	v_add_co_u32_e64 v110, s[8:9], s8, v104
	v_add_co_u32_e64 v112, s[10:11], s10, v104
	v_add_co_u32_e64 v114, s[12:13], s12, v104
	v_add_co_u32_e64 v116, s[14:15], s14, v104
	v_add_co_u32_e64 v118, s[16:17], s16, v104
	s_waitcnt vmcnt(7)
	v_pk_fma_f32 v[28:29], v[200:201], v[44:45], v[28:29] op_sel_hi:[1,0,1]
	s_waitcnt lgkmcnt(13)
	v_pk_fma_f32 v[36:37], v[200:201], v[52:53], v[36:37] op_sel_hi:[1,0,1]
	v_add_co_u32_e64 v120, s[18:19], s18, v104
	v_add_co_u32_e64 v122, s[20:21], s20, v104
	v_add_co_u32_e64 v124, s[22:23], s22, v104
	v_add_co_u32_e64 v126, s[24:25], s24, v104
	v_add_co_u32_e64 v128, s[26:27], s26, v104
	v_add_co_u32_e64 v130, s[28:29], s28, v104
	s_waitcnt vmcnt(6)
	v_pk_fma_f32 v[28:29], v[202:203], v[44:45], v[28:29] op_sel:[0,1,0]
	s_waitcnt lgkmcnt(11)
	v_pk_fma_f32 v[44:45], v[200:201], v[60:61], v[38:39] op_sel_hi:[1,0,1]
	s_waitcnt vmcnt(5)
	v_pk_fma_f32 v[160:161], v[204:205], v[46:47], v[28:29] op_sel_hi:[1,0,1]
	v_pk_fma_f32 v[28:29], v[200:201], v[48:49], v[30:31] op_sel_hi:[1,0,1]
	v_pk_fma_f32 v[28:29], v[202:203], v[48:49], v[28:29] op_sel:[0,1,0]
	v_pk_fma_f32 v[36:37], v[202:203], v[52:53], v[36:37] op_sel:[0,1,0]
	v_pk_fma_f32 v[44:45], v[202:203], v[60:61], v[44:45] op_sel:[0,1,0]
	v_pk_fma_f32 v[48:49], v[204:205], v[50:51], v[28:29] op_sel_hi:[1,0,1]
	v_mov_b32_e32 v50, v55
	v_pk_fma_f32 v[52:53], v[204:205], v[54:55], v[36:37] op_sel_hi:[1,0,1]
	v_pk_fma_f32 v[54:55], v[204:205], v[62:63], v[44:45] op_sel_hi:[1,0,1]
	v_mov_b32_e32 v154, v63
	ds_read_b128 v[28:31], v107 offset:80
	ds_read_b128 v[36:39], v107 offset:4176
	ds_read_b128 v[44:47], v107 offset:8272
	ds_read_b128 v[60:63], v107 offset:12368
	v_add_co_u32_e64 v132, s[30:31], s30, v104
	v_add_co_u32_e64 v134, s[34:35], s34, v104
	v_add_co_u32_e64 v136, s[36:37], s36, v104
	v_add_co_u32_e64 v138, s[38:39], s38, v104
	v_add_co_u32_e64 v140, s[40:41], s40, v104
	v_add_co_u32_e64 v142, s[42:43], s42, v104
	v_add_co_u32_e64 v144, s[44:45], s44, v104
	v_add_co_u32_e64 v146, s[48:49], s48, v104
	v_add_co_u32_e64 v148, s[50:51], s50, v104
	v_add_co_u32_e64 v150, s[52:53], s52, v104
	v_add_co_u32_e64 v104, s[54:55], s54, v104
	s_add_u32 s96, s96, 0xc0000
	s_addc_u32 s97, s97, 0
	s_addk_i32 s1, 0x80
	s_cmp_lg_u32 s96, 0x300000
	s_waitcnt vmcnt(4)
	v_pk_fma_f32 v[156:157], v[206:207], v[162:163], v[160:161] op_sel_hi:[1,0,1]
	v_pk_fma_f32 v[158:159], v[206:207], v[168:169], v[48:49] op_sel_hi:[1,0,1]
	v_pk_fma_f32 v[160:161], v[206:207], v[50:51], v[52:53] op_sel_hi:[1,0,1]
	ds_read_b128 v[48:51], v107 offset:96
	v_pk_fma_f32 v[152:153], v[206:207], v[154:155], v[54:55] op_sel_hi:[1,0,1]
	ds_read_b128 v[52:55], v107 offset:4192
	s_nop 0
	s_nop 0
	v_mov_b32_e32 v162, v89
	s_waitcnt vmcnt(3)
	v_pk_fma_f32 v[154:155], v[208:209], v[72:73], v[156:157] op_sel_hi:[1,0,1]
	s_waitcnt vmcnt(2)
	v_pk_fma_f32 v[72:73], v[210:211], v[72:73], v[154:155] op_sel:[0,1,0]
	v_mov_b32_e32 v156, v75
	s_waitcnt vmcnt(1)
	v_pk_fma_f32 v[154:155], v[212:213], v[74:75], v[72:73] op_sel_hi:[1,0,1]
	v_pk_fma_f32 v[72:73], v[208:209], v[86:87], v[158:159] op_sel_hi:[1,0,1]
	s_nop 0
	v_pk_fma_f32 v[72:73], v[210:211], v[86:87], v[72:73] op_sel:[0,1,0]
	v_pk_fma_f32 v[86:87], v[208:209], v[76:77], v[160:161] op_sel_hi:[1,0,1]
	s_waitcnt lgkmcnt(14)
	v_pk_fma_f32 v[80:81], v[208:209], v[82:83], v[152:153] op_sel_hi:[1,0,1]
	v_pk_fma_f32 v[76:77], v[210:211], v[76:77], v[86:87] op_sel:[0,1,0]
	v_pk_fma_f32 v[80:81], v[210:211], v[82:83], v[80:81] op_sel:[0,1,0]
	v_pk_fma_f32 v[88:89], v[212:213], v[88:89], v[72:73] op_sel_hi:[1,0,1]
	v_pk_fma_f32 v[158:159], v[212:213], v[78:79], v[76:77] op_sel_hi:[1,0,1]
	v_pk_fma_f32 v[92:93], v[212:213], v[84:85], v[80:81] op_sel_hi:[1,0,1]
	v_mov_b32_e32 v152, v79
	v_mov_b32_e32 v160, v85
	ds_read_b128 v[72:75], v107 offset:8288
	ds_read_b128 v[76:79], v107 offset:12384
	ds_read_b128 v[80:83], v107 offset:112
	ds_read_b128 v[84:87], v107 offset:4208
	s_waitcnt vmcnt(0)
	v_pk_fma_f32 v[168:169], v[214:215], v[156:157], v[154:155] op_sel_hi:[1,0,1]
	v_pk_fma_f32 v[170:171], v[214:215], v[162:163], v[88:89] op_sel_hi:[1,0,1]
	v_pk_fma_f32 v[172:173], v[214:215], v[152:153], v[158:159] op_sel_hi:[1,0,1]
	ds_read_b128 v[88:91], v107 offset:8304
	v_pk_fma_f32 v[174:175], v[214:215], v[160:161], v[92:93] op_sel_hi:[1,0,1]
	ds_read_b128 v[92:95], v107 offset:12400
	v_addc_co_u32_e64 v107, s[4:5], 0, v105, s[4:5]
	v_addc_co_u32_e64 v109, s[4:5], 0, v105, s[6:7]
	v_addc_co_u32_e64 v111, s[4:5], 0, v105, s[8:9]
	v_addc_co_u32_e64 v113, s[4:5], 0, v105, s[10:11]
	v_addc_co_u32_e64 v115, s[4:5], 0, v105, s[12:13]
	v_addc_co_u32_e64 v117, s[4:5], 0, v105, s[14:15]
	v_addc_co_u32_e64 v119, s[4:5], 0, v105, s[16:17]
	v_addc_co_u32_e64 v121, s[4:5], 0, v105, s[18:19]
	v_addc_co_u32_e64 v123, s[4:5], 0, v105, s[20:21]
	v_addc_co_u32_e64 v125, s[4:5], 0, v105, s[22:23]
	v_addc_co_u32_e64 v127, s[4:5], 0, v105, s[24:25]
	v_addc_co_u32_e64 v129, s[4:5], 0, v105, s[26:27]
	v_addc_co_u32_e64 v131, s[4:5], 0, v105, s[28:29]
	v_addc_co_u32_e64 v133, s[4:5], 0, v105, s[30:31]
	v_addc_co_u32_e64 v135, s[4:5], 0, v105, s[34:35]
	v_addc_co_u32_e64 v137, s[4:5], 0, v105, s[36:37]
	v_addc_co_u32_e64 v139, s[4:5], 0, v105, s[38:39]
	v_addc_co_u32_e64 v141, s[4:5], 0, v105, s[40:41]
	v_addc_co_u32_e64 v143, s[4:5], 0, v105, s[42:43]
	v_addc_co_u32_e64 v145, s[4:5], 0, v105, s[44:45]
	v_addc_co_u32_e64 v147, s[4:5], 0, v105, s[48:49]
	v_addc_co_u32_e64 v149, s[4:5], 0, v105, s[50:51]
	v_addc_co_u32_e64 v151, s[4:5], 0, v105, s[52:53]
	v_addc_co_u32_e64 v105, s[4:5], 0, v105, s[54:55]
	global_load_dwordx2 v[176:177], v[106:107], off
	global_load_dwordx2 v[178:179], v[108:109], off
	global_load_dwordx2 v[180:181], v[110:111], off
	global_load_dwordx2 v[182:183], v[112:113], off
	global_load_dwordx2 v[184:185], v[114:115], off
	global_load_dwordx2 v[162:163], v[116:117], off
	global_load_dwordx2 v[160:161], v[118:119], off
	global_load_dwordx2 v[158:159], v[120:121], off
	global_load_dwordx2 v[156:157], v[122:123], off
	global_load_dwordx2 v[154:155], v[124:125], off
	global_load_dwordx2 v[152:153], v[126:127], off
	s_nop 0
	global_load_dwordx2 v[128:129], v[128:129], off
	s_nop 0
	global_load_dwordx2 v[126:127], v[130:131], off
	global_load_dwordx2 v[124:125], v[132:133], off
	global_load_dwordx2 v[122:123], v[134:135], off
	global_load_dwordx2 v[120:121], v[136:137], off
	global_load_dwordx2 v[118:119], v[138:139], off
	global_load_dwordx2 v[116:117], v[140:141], off
	global_load_dwordx2 v[114:115], v[142:143], off
	global_load_dwordx2 v[112:113], v[144:145], off
	global_load_dwordx2 v[110:111], v[146:147], off
	global_load_dwordx2 v[108:109], v[148:149], off
	global_load_dwordx2 v[106:107], v[150:151], off
	s_nop 0
	global_load_dwordx2 v[104:105], v[104:105], off
	v_mov_b32_e32 v130, v43
	s_waitcnt lgkmcnt(14)
	v_mov_b32_e32 v140, v3
	s_waitcnt lgkmcnt(13)
	v_mov_b32_e32 v142, v19
	s_waitcnt lgkmcnt(12)
	v_mov_b32_e32 v144, v23
	s_waitcnt lgkmcnt(7)
	v_mov_b32_e32 v146, v51
	s_waitcnt lgkmcnt(0)
	v_mov_b32_e32 v148, v95
	s_waitcnt vmcnt(23)
	v_pk_fma_f32 v[132:133], v[176:177], v[40:41], v[168:169] op_sel_hi:[1,0,1]
	v_pk_fma_f32 v[134:135], v[176:177], v[68:69], v[170:171] op_sel_hi:[1,0,1]
	v_pk_fma_f32 v[136:137], v[176:177], v[64:65], v[172:173] op_sel_hi:[1,0,1]
	v_pk_fma_f32 v[138:139], v[176:177], v[56:57], v[174:175] op_sel_hi:[1,0,1]
	s_waitcnt vmcnt(22)
	v_pk_fma_f32 v[40:41], v[178:179], v[40:41], v[132:133] op_sel:[0,1,0]
	v_pk_fma_f32 v[68:69], v[178:179], v[68:69], v[134:135] op_sel:[0,1,0]
	v_pk_fma_f32 v[64:65], v[178:179], v[64:65], v[136:137] op_sel:[0,1,0]
	v_pk_fma_f32 v[56:57], v[178:179], v[56:57], v[138:139] op_sel:[0,1,0]
	s_waitcnt vmcnt(21)
	v_pk_fma_f32 v[40:41], v[180:181], v[42:43], v[40:41] op_sel_hi:[1,0,1]
	v_mov_b32_e32 v42, v71
	v_mov_b32_e32 v132, v67
	v_pk_fma_f32 v[68:69], v[180:181], v[70:71], v[68:69] op_sel_hi:[1,0,1]
	v_mov_b32_e32 v70, v59
	v_pk_fma_f32 v[64:65], v[180:181], v[66:67], v[64:65] op_sel_hi:[1,0,1]
	v_pk_fma_f32 v[56:57], v[180:181], v[58:59], v[56:57] op_sel_hi:[1,0,1]
	s_waitcnt vmcnt(20)
	v_pk_fma_f32 v[40:41], v[182:183], v[130:131], v[40:41] op_sel_hi:[1,0,1]
	v_pk_fma_f32 v[42:43], v[182:183], v[42:43], v[68:69] op_sel_hi:[1,0,1]
	v_pk_fma_f32 v[64:65], v[182:183], v[132:133], v[64:65] op_sel_hi:[1,0,1]
	v_pk_fma_f32 v[56:57], v[182:183], v[70:71], v[56:57] op_sel_hi:[1,0,1]
	s_waitcnt vmcnt(19)
	v_pk_fma_f32 v[40:41], v[184:185], v[4:5], v[40:41] op_sel_hi:[1,0,1]
	v_pk_fma_f32 v[42:43], v[184:185], v[32:33], v[42:43] op_sel_hi:[1,0,1]
	v_pk_fma_f32 v[64:65], v[184:185], v[24:25], v[64:65] op_sel_hi:[1,0,1]
	v_pk_fma_f32 v[56:57], v[184:185], v[0:1], v[56:57] op_sel_hi:[1,0,1]
	s_waitcnt vmcnt(18)
	v_pk_fma_f32 v[4:5], v[162:163], v[4:5], v[40:41] op_sel:[0,1,0]
	v_pk_fma_f32 v[32:33], v[162:163], v[32:33], v[42:43] op_sel:[0,1,0]
	v_pk_fma_f32 v[24:25], v[162:163], v[24:25], v[64:65] op_sel:[0,1,0]
	v_pk_fma_f32 v[0:1], v[162:163], v[0:1], v[56:57] op_sel:[0,1,0]
	v_mov_b32_e32 v134, v7
	v_mov_b32_e32 v66, v35
	v_mov_b32_e32 v136, v27
	s_waitcnt vmcnt(17)
	v_pk_fma_f32 v[4:5], v[160:161], v[6:7], v[4:5] op_sel_hi:[1,0,1]
	v_pk_fma_f32 v[32:33], v[160:161], v[34:35], v[32:33] op_sel_hi:[1,0,1]
	v_pk_fma_f32 v[24:25], v[160:161], v[26:27], v[24:25] op_sel_hi:[1,0,1]
	v_pk_fma_f32 v[0:1], v[160:161], v[2:3], v[0:1] op_sel_hi:[1,0,1]
	s_waitcnt vmcnt(16)
	v_pk_fma_f32 v[2:3], v[158:159], v[134:135], v[4:5] op_sel_hi:[1,0,1]
	v_pk_fma_f32 v[4:5], v[158:159], v[66:67], v[32:33] op_sel_hi:[1,0,1]
	v_pk_fma_f32 v[24:25], v[158:159], v[136:137], v[24:25] op_sel_hi:[1,0,1]
	v_pk_fma_f32 v[0:1], v[158:159], v[140:141], v[0:1] op_sel_hi:[1,0,1]
	s_waitcnt vmcnt(15)
	v_pk_fma_f32 v[2:3], v[156:157], v[8:9], v[2:3] op_sel_hi:[1,0,1]
	v_pk_fma_f32 v[4:5], v[156:157], v[12:13], v[4:5] op_sel_hi:[1,0,1]
	v_pk_fma_f32 v[24:25], v[156:157], v[16:17], v[24:25] op_sel_hi:[1,0,1]
	v_pk_fma_f32 v[0:1], v[156:157], v[20:21], v[0:1] op_sel_hi:[1,0,1]
	s_waitcnt vmcnt(14)
	v_pk_fma_f32 v[2:3], v[154:155], v[8:9], v[2:3] op_sel:[0,1,0]
	v_pk_fma_f32 v[4:5], v[154:155], v[12:13], v[4:5] op_sel:[0,1,0]
	v_pk_fma_f32 v[8:9], v[154:155], v[16:17], v[24:25] op_sel:[0,1,0]
	v_pk_fma_f32 v[0:1], v[154:155], v[20:21], v[0:1] op_sel:[0,1,0]
	v_mov_b32_e32 v138, v11
	v_mov_b32_e32 v58, v15
	s_waitcnt vmcnt(13)
	v_pk_fma_f32 v[2:3], v[152:153], v[10:11], v[2:3] op_sel_hi:[1,0,1]
	v_pk_fma_f32 v[4:5], v[152:153], v[14:15], v[4:5] op_sel_hi:[1,0,1]
	v_pk_fma_f32 v[8:9], v[152:153], v[18:19], v[8:9] op_sel_hi:[1,0,1]
	v_pk_fma_f32 v[0:1], v[152:153], v[22:23], v[0:1] op_sel_hi:[1,0,1]
	s_waitcnt vmcnt(12)
	v_pk_fma_f32 v[2:3], v[128:129], v[138:139], v[2:3] op_sel_hi:[1,0,1]
	v_pk_fma_f32 v[4:5], v[128:129], v[58:59], v[4:5] op_sel_hi:[1,0,1]
	v_pk_fma_f32 v[8:9], v[128:129], v[142:143], v[8:9] op_sel_hi:[1,0,1]
	v_pk_fma_f32 v[0:1], v[128:129], v[144:145], v[0:1] op_sel_hi:[1,0,1]
	s_waitcnt vmcnt(11)
	v_pk_fma_f32 v[2:3], v[126:127], v[28:29], v[2:3] op_sel_hi:[1,0,1]
	v_pk_fma_f32 v[4:5], v[126:127], v[36:37], v[4:5] op_sel_hi:[1,0,1]
	v_pk_fma_f32 v[8:9], v[126:127], v[44:45], v[8:9] op_sel_hi:[1,0,1]
	v_pk_fma_f32 v[0:1], v[126:127], v[60:61], v[0:1] op_sel_hi:[1,0,1]
	s_waitcnt vmcnt(10)
	v_pk_fma_f32 v[2:3], v[124:125], v[28:29], v[2:3] op_sel:[0,1,0]
	v_pk_fma_f32 v[4:5], v[124:125], v[36:37], v[4:5] op_sel:[0,1,0]
	v_pk_fma_f32 v[8:9], v[124:125], v[44:45], v[8:9] op_sel:[0,1,0]
	v_pk_fma_f32 v[0:1], v[124:125], v[60:61], v[0:1] op_sel:[0,1,0]
	v_mov_b32_e32 v130, v31
	v_mov_b32_e32 v68, v39
	v_mov_b32_e32 v132, v47
	v_mov_b32_e32 v70, v63
	s_waitcnt vmcnt(9)
	v_pk_fma_f32 v[2:3], v[122:123], v[30:31], v[2:3] op_sel_hi:[1,0,1]
	v_pk_fma_f32 v[4:5], v[122:123], v[38:39], v[4:5] op_sel_hi:[1,0,1]
	v_pk_fma_f32 v[8:9], v[122:123], v[46:47], v[8:9] op_sel_hi:[1,0,1]
	v_pk_fma_f32 v[0:1], v[122:123], v[62:63], v[0:1] op_sel_hi:[1,0,1]
	s_waitcnt vmcnt(8)
	v_pk_fma_f32 v[2:3], v[120:121], v[130:131], v[2:3] op_sel_hi:[1,0,1]
	v_pk_fma_f32 v[4:5], v[120:121], v[68:69], v[4:5] op_sel_hi:[1,0,1]
	v_pk_fma_f32 v[8:9], v[120:121], v[132:133], v[8:9] op_sel_hi:[1,0,1]
	v_pk_fma_f32 v[0:1], v[120:121], v[70:71], v[0:1] op_sel_hi:[1,0,1]
	s_waitcnt vmcnt(7)
	v_pk_fma_f32 v[2:3], v[118:119], v[48:49], v[2:3] op_sel_hi:[1,0,1]
	v_pk_fma_f32 v[4:5], v[118:119], v[52:53], v[4:5] op_sel_hi:[1,0,1]
	v_pk_fma_f32 v[8:9], v[118:119], v[72:73], v[8:9] op_sel_hi:[1,0,1]
	v_pk_fma_f32 v[0:1], v[118:119], v[76:77], v[0:1] op_sel_hi:[1,0,1]
	s_waitcnt vmcnt(6)
	v_pk_fma_f32 v[2:3], v[116:117], v[48:49], v[2:3] op_sel:[0,1,0]
	v_pk_fma_f32 v[4:5], v[116:117], v[52:53], v[4:5] op_sel:[0,1,0]
	v_pk_fma_f32 v[8:9], v[116:117], v[72:73], v[8:9] op_sel:[0,1,0]
	v_pk_fma_f32 v[0:1], v[116:117], v[76:77], v[0:1] op_sel:[0,1,0]
	v_mov_b32_e32 v6, v55
	v_mov_b32_e32 v40, v75
	v_mov_b32_e32 v34, v79
	s_waitcnt vmcnt(5)
	v_pk_fma_f32 v[2:3], v[114:115], v[50:51], v[2:3] op_sel_hi:[1,0,1]
	v_pk_fma_f32 v[4:5], v[114:115], v[54:55], v[4:5] op_sel_hi:[1,0,1]
	v_pk_fma_f32 v[8:9], v[114:115], v[74:75], v[8:9] op_sel_hi:[1,0,1]
	v_pk_fma_f32 v[0:1], v[114:115], v[78:79], v[0:1] op_sel_hi:[1,0,1]
	s_waitcnt vmcnt(4)
	v_pk_fma_f32 v[2:3], v[112:113], v[146:147], v[2:3] op_sel_hi:[1,0,1]
	v_pk_fma_f32 v[4:5], v[112:113], v[6:7], v[4:5] op_sel_hi:[1,0,1]
	v_pk_fma_f32 v[6:7], v[112:113], v[40:41], v[8:9] op_sel_hi:[1,0,1]
	v_pk_fma_f32 v[0:1], v[112:113], v[34:35], v[0:1] op_sel_hi:[1,0,1]
	s_waitcnt vmcnt(3)
	v_pk_fma_f32 v[2:3], v[110:111], v[80:81], v[2:3] op_sel_hi:[1,0,1]
	v_pk_fma_f32 v[4:5], v[110:111], v[84:85], v[4:5] op_sel_hi:[1,0,1]
	v_pk_fma_f32 v[6:7], v[110:111], v[88:89], v[6:7] op_sel_hi:[1,0,1]
	v_pk_fma_f32 v[0:1], v[110:111], v[92:93], v[0:1] op_sel_hi:[1,0,1]
	s_waitcnt vmcnt(2)
	v_pk_fma_f32 v[2:3], v[108:109], v[80:81], v[2:3] op_sel:[0,1,0]
	v_pk_fma_f32 v[4:5], v[108:109], v[84:85], v[4:5] op_sel:[0,1,0]
	v_pk_fma_f32 v[6:7], v[108:109], v[88:89], v[6:7] op_sel:[0,1,0]
	v_pk_fma_f32 v[0:1], v[108:109], v[92:93], v[0:1] op_sel:[0,1,0]
	v_mov_b32_e32 v42, v83
	v_mov_b32_e32 v26, v87
	v_mov_b32_e32 v64, v91
	s_waitcnt vmcnt(1)
	v_pk_fma_f32 v[2:3], v[106:107], v[82:83], v[2:3] op_sel_hi:[1,0,1]
	v_pk_fma_f32 v[4:5], v[106:107], v[86:87], v[4:5] op_sel_hi:[1,0,1]
	v_pk_fma_f32 v[6:7], v[106:107], v[90:91], v[6:7] op_sel_hi:[1,0,1]
	v_pk_fma_f32 v[0:1], v[106:107], v[94:95], v[0:1] op_sel_hi:[1,0,1]
	s_waitcnt vmcnt(0)
	v_pk_fma_f32 v[28:29], v[104:105], v[42:43], v[2:3] op_sel_hi:[1,0,1]
	v_pk_fma_f32 v[30:31], v[104:105], v[26:27], v[4:5] op_sel_hi:[1,0,1]
	v_pk_fma_f32 v[36:37], v[104:105], v[64:65], v[6:7] op_sel_hi:[1,0,1]
	v_pk_fma_f32 v[38:39], v[104:105], v[148:149], v[0:1] op_sel_hi:[1,0,1]
	s_cbranch_scc1 .LBB0_24
	v_add_u32_e32 v0, 0x4000, v165
	ds_write2_b64 v0, v[28:29], v[30:31] offset1:48
	ds_write2_b64 v0, v[36:37], v[38:39] offset0:96 offset1:144
